# phase-2 RG-LRU gate math: per-channel constants folded (sigmoid argument as one fma with pre-scaled bias, decay exponent as one multiply with pre-scaled softplus): 122 fewer VALU per unit, f32 through
# speedup vs baseline: 1.0048x; 1.0040x over previous
; template <bool FINAL>
; __device__ __forceinline__ void lru_unit(const Args& a, unsigned char* lds_g, int b, int cidx, int blk, int tid, bf16x8_t (&wl)[2][2][4], int& wl_blk) {
;     ...
;         for (int q = 0; q < 4; ++q) { const f32x4 bv = *(const f32x4*)(a.in[I_CONVB] + ch0 + 4 * q); z[4 * q] = bv.x; z[4 * q + 1] = bv.y; z[4 * q + 2] = bv.z; z[4 * q + 3] = bv.w; }
;         v4u ua[4], ub[4]; float msk[4];
; #pragma unroll
;         for (int w4 = 0; w4 < 4; ++w4) { const int pp = p + w4 - 2; const bool ok = pp >= 0 && pp < seglen; const int ppc = ok ? pp : p;
;             const v4u* src = (const v4u*)(UX + (size_t)lru_pos_row(b, isctx, ppc) * 1024 + ch0); ua[w4] = src[0]; ub[w4] = src[1]; msk[w4] = ok ? 1.f : 0.f; }
; #pragma unroll
;         for (int w4 = 0; w4 < 4; ++w4) { const float* cw = a.in[I_CONVW] + w4 * 1024 + ch0;
;             const unsigned uu[8] = {ua[w4].x, ua[w4].y, ua[w4].z, ua[w4].w, ub[w4].x, ub[w4].y, ub[w4].z, ub[w4].w};
; #pragma unroll
;             for (int q = 0; q < 4; ++q) { const f32x4 cv = *(const f32x4*)(cw + 4 * q) * msk[w4]; z[4 * q] += cv.x * bflo(uu[2 * q]); z[4 * q + 1] += cv.y * bfhi(uu[2 * q]); z[4 * q + 2] += cv.z * bflo(uu[2 * q + 1]); z[4 * q + 3] += cv.w * bfhi(uu[2 * q + 1]); } }
;     ...
;         const float ba = gba[d], bx = gbx[d], lam = glam[d];
.Lp2pf_skip:
	s_mov_b32 s92, 0xbfb8aa3b
	v_mul_f32_e32 v134, 0xbfb8aa3b, v134
	v_mul_f32_e32 v135, 0xbfb8aa3b, v135
	v_mul_f32_e32 v191, 0xbfb8aa3b, v191
	v_mul_f32_e32 v192, 0xbfb8aa3b, v192
	v_lshlrev_b32_e32 v210, 16, v88
	v_and_b32_e32 v211, 0xffff0000, v88
	v_lshlrev_b32_e32 v88, 16, v89
	v_and_b32_e32 v89, 0xffff0000, v89
	v_cndmask_b32_e64 v104, 0, 1.0, vcc
	v_lshlrev_b32_e32 v212, 16, v96
	v_and_b32_e32 v213, 0xffff0000, v96
	v_lshlrev_b32_e32 v96, 16, v97
	v_and_b32_e32 v97, 0xffff0000, v97
	v_lshlrev_b32_e32 v214, 16, v100
	v_and_b32_e32 v215, 0xffff0000, v100
	v_lshlrev_b32_e32 v100, 16, v101
	v_and_b32_e32 v101, 0xffff0000, v101
	v_cndmask_b32_e64 v208, 0, 1.0, s[6:7]
	v_cmp_ngt_f32_e32 vcc, s35, v131
	v_pk_mul_f32 v[116:117], v[206:207], v[116:117] op_sel_hi:[0,1]
	v_pk_mul_f32 v[114:115], v[206:207], v[114:115] op_sel_hi:[0,1]
	v_pk_fma_f32 v[88:89], v[116:117], v[88:89], v[94:95]
	v_pk_fma_f32 v[92:93], v[114:115], v[210:211], v[92:93]
	v_pk_mul_f32 v[126:127], v[206:207], v[138:139] op_sel_hi:[0,1]
	v_pk_mul_f32 v[94:95], v[112:113], v[142:143] op_sel_hi:[0,1]
	v_pk_mul_f32 v[114:115], v[112:113], v[140:141] op_sel_hi:[0,1]
	v_pk_mul_f32 v[116:117], v[112:113], v[146:147] op_sel_hi:[0,1]
	v_pk_mul_f32 v[138:139], v[112:113], v[144:145] op_sel_hi:[0,1]
	v_pk_mul_f32 v[140:141], v[112:113], v[150:151] op_sel_hi:[0,1]
	v_pk_mul_f32 v[142:143], v[112:113], v[148:149] op_sel_hi:[0,1]
	v_pk_mul_f32 v[108:109], v[112:113], v[108:109] op_sel_hi:[0,1]
	v_pk_mul_f32 v[106:107], v[112:113], v[106:107] op_sel_hi:[0,1]
	v_pk_mul_f32 v[112:113], v[104:105], v[154:155] op_sel_hi:[0,1]
	v_pk_fma_f32 v[88:89], v[94:95], v[96:97], v[88:89]
	v_pk_mul_f32 v[118:119], v[206:207], v[118:119] op_sel_hi:[0,1]
	v_pk_fma_f32 v[88:89], v[112:113], v[100:101], v[88:89]
	v_lshlrev_b32_e32 v100, 16, v90
	v_and_b32_e32 v101, 0xffff0000, v90
	v_pk_fma_f32 v[80:81], v[118:119], v[100:101], v[80:81]
	v_lshlrev_b32_e32 v100, 16, v98
	v_and_b32_e32 v101, 0xffff0000, v98
	v_pk_mul_f32 v[148:149], v[104:105], v[156:157] op_sel_hi:[0,1]
	v_pk_fma_f32 v[80:81], v[138:139], v[100:101], v[80:81]
	v_lshlrev_b32_e32 v100, 16, v102
	v_and_b32_e32 v101, 0xffff0000, v102
	v_pk_mul_f32 v[96:97], v[208:209], v[176:177] op_sel_hi:[0,1]
	v_pk_fma_f32 v[80:81], v[148:149], v[100:101], v[80:81]
	v_lshlrev_b32_e32 v100, 16, v174
	v_and_b32_e32 v101, 0xffff0000, v174
	v_pk_mul_f32 v[120:121], v[206:207], v[120:121] op_sel_hi:[0,1]
	v_pk_mul_f32 v[136:137], v[206:207], v[136:137] op_sel_hi:[0,1]
	v_pk_fma_f32 v[80:81], v[96:97], v[100:101], v[80:81]
	v_lshlrev_b32_e32 v90, 16, v91
	v_and_b32_e32 v91, 0xffff0000, v91
	v_lshlrev_b32_e32 v96, 16, v72
	v_and_b32_e32 v97, 0xffff0000, v72
	v_lshlrev_b32_e32 v72, 16, v73
	v_and_b32_e32 v73, 0xffff0000, v73
	v_pk_fma_f32 v[82:83], v[120:121], v[90:91], v[82:83]
	v_lshlrev_b32_e32 v90, 16, v99
	v_and_b32_e32 v91, 0xffff0000, v99
	v_pk_fma_f32 v[68:69], v[136:137], v[96:97], v[68:69]
	v_lshlrev_b32_e32 v96, 16, v76
	v_and_b32_e32 v97, 0xffff0000, v76
	v_pk_fma_f32 v[70:71], v[126:127], v[72:73], v[70:71]
	v_lshlrev_b32_e32 v72, 16, v77
	v_and_b32_e32 v73, 0xffff0000, v77
	v_pk_mul_f32 v[124:125], v[206:207], v[124:125] op_sel_hi:[0,1]
	v_pk_mul_f32 v[146:147], v[104:105], v[158:159] op_sel_hi:[0,1]
	v_pk_mul_f32 v[154:155], v[104:105], v[162:163] op_sel_hi:[0,1]
	v_pk_mul_f32 v[156:157], v[208:209], v[170:171] op_sel_hi:[0,1]
	v_lshlrev_b32_e32 v162, 16, v173
	v_and_b32_e32 v163, 0xffff0000, v173
	v_pk_fma_f32 v[82:83], v[116:117], v[90:91], v[82:83]
	v_lshlrev_b32_e32 v90, 16, v103
	v_and_b32_e32 v91, 0xffff0000, v103
	v_pk_fma_f32 v[68:69], v[142:143], v[96:97], v[68:69]
	v_lshlrev_b32_e32 v96, 16, v84
	v_and_b32_e32 v97, 0xffff0000, v84
	v_pk_fma_f32 v[70:71], v[140:141], v[72:73], v[70:71]
	v_lshlrev_b32_e32 v72, 16, v85
	v_and_b32_e32 v73, 0xffff0000, v85
	v_lshlrev_b32_e32 v84, 16, v74
	v_and_b32_e32 v85, 0xffff0000, v74
	v_lshlrev_b32_e32 v74, 16, v75
	v_and_b32_e32 v75, 0xffff0000, v75
	v_pk_mul_f32 v[122:123], v[206:207], v[122:123] op_sel_hi:[0,1]
	v_pk_mul_f32 v[150:151], v[104:105], v[166:167] op_sel_hi:[0,1]
	v_pk_fma_f32 v[94:95], v[156:157], v[162:163], v[88:89]
	v_pk_mul_f32 v[88:89], v[208:209], v[178:179] op_sel_hi:[0,1]
	v_pk_fma_f32 v[82:83], v[146:147], v[90:91], v[82:83]
	v_lshlrev_b32_e32 v90, 16, v175
	v_and_b32_e32 v91, 0xffff0000, v175
	v_pk_fma_f32 v[66:67], v[124:125], v[74:75], v[66:67]
	v_lshlrev_b32_e32 v74, 16, v79
	v_and_b32_e32 v75, 0xffff0000, v79
	v_pk_fma_f32 v[82:83], v[88:89], v[90:91], v[82:83]
	v_pk_mul_f32 v[88:89], v[208:209], v[200:201] op_sel_hi:[0,1]
	v_pk_fma_f32 v[70:71], v[150:151], v[72:73], v[70:71]
	v_lshlrev_b32_e32 v72, 16, v195
	v_and_b32_e32 v73, 0xffff0000, v195
	v_pk_fma_f32 v[64:65], v[122:123], v[84:85], v[64:65]
	v_lshlrev_b32_e32 v84, 16, v78
	v_and_b32_e32 v85, 0xffff0000, v78
	v_pk_fma_f32 v[66:67], v[108:109], v[74:75], v[66:67]
	v_lshlrev_b32_e32 v74, 16, v87
	v_and_b32_e32 v75, 0xffff0000, v87
	v_pk_mul_f32 v[144:145], v[104:105], v[152:153] op_sel_hi:[0,1]
	v_pk_mul_f32 v[152:153], v[104:105], v[164:165] op_sel_hi:[0,1]
	v_pk_mul_f32 v[104:105], v[104:105], v[160:161] op_sel_hi:[0,1]
	v_pk_fma_f32 v[70:71], v[88:89], v[72:73], v[70:71]
	v_pk_mul_f32 v[72:73], v[208:209], v[204:205] op_sel_hi:[0,1]
	v_pk_fma_f32 v[64:65], v[106:107], v[84:85], v[64:65]
	v_lshlrev_b32_e32 v84, 16, v86
	v_and_b32_e32 v85, 0xffff0000, v86
	v_pk_fma_f32 v[66:67], v[154:155], v[74:75], v[66:67]
	v_lshlrev_b32_e32 v74, 16, v197
	v_and_b32_e32 v75, 0xffff0000, v197
	v_pk_fma_f32 v[92:93], v[114:115], v[212:213], v[92:93]
	v_pk_mul_f32 v[76:77], v[208:209], v[202:203] op_sel_hi:[0,1]
; #define WG_BAR() do { asm volatile("s_waitcnt lgkmcnt(0)" ::: "memory"); __builtin_amdgcn_s_barrier(); asm volatile("" ::: "memory"); } while (0)
; __device__ __forceinline__ unsigned pk2(float lo, float hi) { return pg8::cvt_pk_bf16(lo, hi); }
; template <bool FINAL>
; __device__ __forceinline__ void lru_unit(const Args& a, unsigned char* lds_g, int b, int cidx, int blk, int tid, bf16x8_t (&wl)[2][2][4], int& wl_blk) {
;     ...
;         for (int q = 0; q < 4; ++q) *(f32x4*)(zf + pos * 132 + cg * 16 + 4 * q) = (f32x4){z[4 * q], z[4 * q + 1], z[4 * q + 2], z[4 * q + 3]};
;         v4u o0, o1; o0.x = pk2(z[0], z[1]); o0.y = pk2(z[2], z[3]); o0.z = pk2(z[4], z[5]); o0.w = pk2(z[6], z[7]); o1.x = pk2(z[8], z[9]); o1.y = pk2(z[10], z[11]); o1.z = pk2(z[12], z[13]); o1.w = pk2(z[14], z[15]);
;         *(v4u*)(zb + pos * 136 + cg * 16) = o0; *(v4u*)(zb + pos * 136 + cg * 16 + 8) = o1;
;     }
;     WG_BAR();
;     f32x4 acc[2][2][4];
; #pragma unroll
;     for (int d = 0; d < 2; ++d)
; #pragma unroll
;         for (int m = 0; m < 2; ++m)
; #pragma unroll
;             for (int mt = 0; mt < 4; ++mt) acc[d][m][mt] = (f32x4){0.f, 0.f, 0.f, 0.f};
; #pragma unroll
;     for (int ks = 0; ks < 4; ++ks) {
;         bf16x8_t af[4];
; #pragma unroll
;         for (int mt = 0; mt < 4; ++mt) af[mt] = *(const bf16x8_t*)(zb + (16 * mt + fr) * 136 + 32 * ks + 8 * fq);
; #pragma unroll
;         for (int d = 0; d < 2; ++d)
; #pragma unroll
;             for (int m = 0; m < 2; ++m) {
; #pragma unroll
;                 for (int mt = 0; mt < 4; ++mt) acc[d][m][mt] = __builtin_amdgcn_mfma_f32_16x16x32_bf16(af[mt], wl[d][m][ks], acc[d][m][mt], 0, 0, 0); }
;     }
;     const int chl = 16 * w + fr, ch = blk * 128 + chl;
;     float hsum[4][4];
; #pragma unroll
;     for (int d = 0; d < 2; ++d) {
;         const float ba = gba[d], bx = gbx[d], lam = glam[d];
;         const float sp = (-lam > 20.f) ? -lam : log1pf(__expf(-lam));
	v_pk_fma_f32 v[64:65], v[104:105], v[84:85], v[64:65]
	v_lshlrev_b32_e32 v84, 16, v196
	v_and_b32_e32 v85, 0xffff0000, v196
	v_pk_fma_f32 v[66:67], v[72:73], v[74:75], v[66:67]
	v_mul_lo_u32 v72, v111, s33
	v_pk_mul_f32 v[158:159], v[208:209], v[168:169] op_sel_hi:[0,1]
	v_lshlrev_b32_e32 v160, 16, v172
	v_and_b32_e32 v161, 0xffff0000, v172
	v_pk_fma_f32 v[92:93], v[144:145], v[214:215], v[92:93]
	v_pk_mul_f32 v[90:91], v[208:209], v[198:199] op_sel_hi:[0,1]
	v_pk_fma_f32 v[68:69], v[152:153], v[96:97], v[68:69]
	v_lshlrev_b32_e32 v96, 16, v194
	v_and_b32_e32 v97, 0xffff0000, v194
	v_pk_fma_f32 v[64:65], v[76:77], v[84:85], v[64:65]
	v_add_u32_e32 v76, 0, v72
	v_pk_fma_f32 v[92:93], v[158:159], v[160:161], v[92:93]
	v_pk_fma_f32 v[68:69], v[90:91], v[96:97], v[68:69]
	v_lshl_add_u32 v72, v110, 2, v76
	ds_write_b128 v72, v[92:95]
	ds_write_b128 v72, v[80:83] offset:16
	ds_write_b128 v72, v[68:71] offset:32
	ds_write_b128 v72, v[64:67] offset:48
	v_cvt_pk_bf16_f32 v68, v68, v69
	v_cvt_pk_bf16_f32 v69, v70, v71
	v_cvt_pk_bf16_f32 v70, v64, v65
	v_lshlrev_b32_e32 v64, 8, v111
	v_sub_u32_e32 v64, v76, v64
	v_cvt_pk_bf16_f32 v72, v92, v93
	v_cvt_pk_bf16_f32 v73, v94, v95
	v_cvt_pk_bf16_f32 v74, v80, v81
	v_cvt_pk_bf16_f32 v75, v82, v83
	v_lshl_add_u32 v64, v110, 1, v64
	v_cvt_pk_bf16_f32 v71, v66, v67
	ds_write_b128 v64, v[72:75] offset:33792
	ds_write_b128 v64, v[68:71] offset:33808
	v_and_b32_e32 v64, 48, v189
	v_add_u32_e32 v92, 0, v64
	s_waitcnt lgkmcnt(0)
	s_barrier
	v_mad_u32_u24 v133, v188, s34, v92
	v_or_b32_e32 v93, 48, v189
	ds_read_b128 v[64:67], v133 offset:33792
	ds_read_b128 v[68:71], v133 offset:38144
	ds_read_b128 v[72:75], v133 offset:33856
	ds_read_b128 v[80:83], v133 offset:42496
	ds_read_b128 v[84:87], v133 offset:38208
	v_mad_u32_u24 v164, v93, s34, v92
	ds_read_b128 v[92:95], v133 offset:42560
	ds_read_b128 v[100:103], v164 offset:33792
	ds_read_b128 v[104:107], v164 offset:33856
	s_waitcnt lgkmcnt(7)
	v_mfma_f32_16x16x32_bf16 v[76:79], v[64:67], v[0:3], 0
	s_waitcnt lgkmcnt(6)
	v_mfma_f32_16x16x32_bf16 v[88:91], v[68:71], v[0:3], 0
	s_waitcnt lgkmcnt(4)
	v_mfma_f32_16x16x32_bf16 v[96:99], v[80:83], v[0:3], 0
	s_waitcnt lgkmcnt(1)
	v_mfma_f32_16x16x32_bf16 v[108:111], v[100:103], v[0:3], 0
	v_mfma_f32_16x16x32_bf16 v[112:115], v[64:67], v[16:19], 0
	v_mfma_f32_16x16x32_bf16 v[116:119], v[68:71], v[16:19], 0
	v_mfma_f32_16x16x32_bf16 v[120:123], v[80:83], v[16:19], 0
	v_mfma_f32_16x16x32_bf16 v[124:127], v[100:103], v[16:19], 0
	v_mfma_f32_16x16x32_bf16 v[136:139], v[64:67], v[32:35], 0
	v_mfma_f32_16x16x32_bf16 v[140:143], v[68:71], v[32:35], 0
	v_mfma_f32_16x16x32_bf16 v[144:147], v[80:83], v[32:35], 0
	v_mfma_f32_16x16x32_bf16 v[148:151], v[100:103], v[32:35], 0
	v_mfma_f32_16x16x32_bf16 v[64:67], v[64:67], v[48:51], 0
	v_mfma_f32_16x16x32_bf16 v[68:71], v[68:71], v[48:51], 0
	v_mfma_f32_16x16x32_bf16 v[80:83], v[80:83], v[48:51], 0
	v_mfma_f32_16x16x32_bf16 v[100:103], v[100:103], v[48:51], 0
	v_mfma_f32_16x16x32_bf16 v[76:79], v[72:75], v[4:7], v[76:79]
	v_mfma_f32_16x16x32_bf16 v[88:91], v[84:87], v[4:7], v[88:91]
	v_mfma_f32_16x16x32_bf16 v[96:99], v[92:95], v[4:7], v[96:99]
	s_waitcnt lgkmcnt(0)
	v_mfma_f32_16x16x32_bf16 v[108:111], v[104:107], v[4:7], v[108:111]
	v_mfma_f32_16x16x32_bf16 v[112:115], v[72:75], v[20:23], v[112:115]
	v_mfma_f32_16x16x32_bf16 v[116:119], v[84:87], v[20:23], v[116:119]
	v_mfma_f32_16x16x32_bf16 v[120:123], v[92:95], v[20:23], v[120:123]
	v_mfma_f32_16x16x32_bf16 v[124:127], v[104:107], v[20:23], v[124:127]
	v_mfma_f32_16x16x32_bf16 v[136:139], v[72:75], v[36:39], v[136:139]
	v_mfma_f32_16x16x32_bf16 v[140:143], v[84:87], v[36:39], v[140:143]
	v_mfma_f32_16x16x32_bf16 v[144:147], v[92:95], v[36:39], v[144:147]
	v_mfma_f32_16x16x32_bf16 v[148:151], v[104:107], v[36:39], v[148:151]
	v_mfma_f32_16x16x32_bf16 v[64:67], v[72:75], v[52:55], v[64:67]
	v_mfma_f32_16x16x32_bf16 v[68:71], v[84:87], v[52:55], v[68:71]
	ds_read_b128 v[84:87], v133 offset:33920
	ds_read_b128 v[152:155], v133 offset:33984
	v_mfma_f32_16x16x32_bf16 v[72:75], v[92:95], v[52:55], v[80:83]
	ds_read_b128 v[92:95], v133 offset:38272
	ds_read_b128 v[156:159], v133 offset:38336
	v_mfma_f32_16x16x32_bf16 v[80:83], v[104:107], v[52:55], v[100:103]
	s_nop 2
	ds_read_b128 v[100:103], v133 offset:42624
	ds_read_b128 v[160:163], v133 offset:42688
	ds_read_b128 v[104:107], v164 offset:33920
	ds_read_b128 v[164:167], v164 offset:33984
	s_waitcnt lgkmcnt(7)
	v_mfma_f32_16x16x32_bf16 v[76:79], v[84:87], v[8:11], v[76:79]
	s_waitcnt lgkmcnt(5)
	v_mfma_f32_16x16x32_bf16 v[88:91], v[92:95], v[8:11], v[88:91]
	s_waitcnt lgkmcnt(3)
	v_mfma_f32_16x16x32_bf16 v[96:99], v[100:103], v[8:11], v[96:99]
	s_waitcnt lgkmcnt(1)
	v_mfma_f32_16x16x32_bf16 v[168:171], v[104:107], v[8:11], v[108:111]
	v_mfma_f32_16x16x32_bf16 v[112:115], v[84:87], v[24:27], v[112:115]
	v_mfma_f32_16x16x32_bf16 v[172:175], v[92:95], v[24:27], v[116:119]
	v_mfma_f32_16x16x32_bf16 v[176:179], v[100:103], v[24:27], v[120:123]
	v_mfma_f32_16x16x32_bf16 v[194:197], v[104:107], v[24:27], v[124:127]
	v_mfma_f32_16x16x32_bf16 v[136:139], v[84:87], v[40:43], v[136:139]
	v_mfma_f32_16x16x32_bf16 v[140:143], v[92:95], v[40:43], v[140:143]
	v_mfma_f32_16x16x32_bf16 v[144:147], v[100:103], v[40:43], v[144:147]
	v_mfma_f32_16x16x32_bf16 v[148:151], v[104:107], v[40:43], v[148:151]
	v_mfma_f32_16x16x32_bf16 v[64:67], v[84:87], v[56:59], v[64:67]
	v_mfma_f32_16x16x32_bf16 v[198:201], v[92:95], v[56:59], v[68:71]
	v_mfma_f32_16x16x32_bf16 v[72:75], v[100:103], v[56:59], v[72:75]
	v_mfma_f32_16x16x32_bf16 v[202:205], v[104:107], v[56:59], v[80:83]
	v_mfma_f32_16x16x32_bf16 v[124:127], v[152:155], v[12:15], v[76:79]
	v_mfma_f32_16x16x32_bf16 v[116:119], v[156:159], v[12:15], v[88:91]
	v_mfma_f32_16x16x32_bf16 v[108:111], v[160:163], v[12:15], v[96:99]
	s_waitcnt lgkmcnt(0)
	v_mfma_f32_16x16x32_bf16 v[100:103], v[164:167], v[12:15], v[168:171]
	v_mfma_f32_16x16x32_bf16 v[120:123], v[152:155], v[28:31], v[112:115]
	v_mfma_f32_16x16x32_bf16 v[112:115], v[156:159], v[28:31], v[172:175]
	v_mfma_f32_16x16x32_bf16 v[104:107], v[160:163], v[28:31], v[176:179]
	v_mfma_f32_16x16x32_bf16 v[96:99], v[164:167], v[28:31], v[194:197]
	v_mfma_f32_16x16x32_bf16 v[92:95], v[152:155], v[44:47], v[136:139]
	v_mfma_f32_16x16x32_bf16 v[84:87], v[156:159], v[44:47], v[140:143]
	s_nop 1
	v_xor_b32_e32 v138, 0x80000000, v131
	v_mfma_f32_16x16x32_bf16 v[76:79], v[160:163], v[44:47], v[144:147]
	v_mfma_f32_16x16x32_bf16 v[68:71], v[164:167], v[44:47], v[148:151]
	v_mfma_f32_16x16x32_bf16 v[88:91], v[152:155], v[60:63], v[64:67]
	v_mfma_f32_16x16x32_bf16 v[80:83], v[156:159], v[60:63], v[198:201]
	v_mfma_f32_16x16x32_bf16 v[72:75], v[160:163], v[60:63], v[72:75]
	v_mfma_f32_16x16x32_bf16 v[64:67], v[164:167], v[60:63], v[202:205]
	s_and_saveexec_b64 s[4:5], vcc
	s_cbranch_execz .LBB0_305
; template <bool FINAL>
; __device__ __forceinline__ void lru_unit(const Args& a, unsigned char* lds_g, int b, int cidx, int blk, int tid, bf16x8_t (&wl)[2][2][4], int& wl_blk) {
;     ...
;         const float sp = (-lam > 20.f) ? -lam : log1pf(__expf(-lam));
	v_mul_f32_e32 v131, 0xbfb8aa3b, v131
	v_exp_f32_e32 v133, v131
	s_nop 0
	v_add_f32_e32 v131, 1.0, v133
	v_frexp_mant_f32_e32 v139, v131
	v_cvt_f64_f32_e32 v[136:137], v131
	v_add_f32_e32 v138, -1.0, v131
	v_frexp_exp_i32_f64_e32 v136, v[136:137]
	v_cmp_gt_f32_e32 vcc, s36, v139
	v_sub_f32_e32 v140, v138, v131
	v_sub_f32_e32 v138, v133, v138
	v_subbrev_co_u32_e32 v144, vcc, 0, v136, vcc
	v_add_f32_e32 v140, 1.0, v140
	v_sub_u32_e32 v136, 0, v144
	v_add_f32_e32 v138, v138, v140
	v_ldexp_f32 v131, v131, v136
	v_ldexp_f32 v136, v138, v136
	v_add_f32_e32 v138, -1.0, v131
	v_add_f32_e32 v137, 1.0, v138
	v_sub_f32_e32 v137, v131, v137
	v_add_f32_e32 v139, v136, v137
	v_add_f32_e32 v137, 1.0, v131
	v_add_f32_e32 v140, -1.0, v137
	v_sub_f32_e32 v131, v131, v140
	v_add_f32_e32 v131, v136, v131
	v_add_f32_e32 v145, v137, v131
	v_rcp_f32_e32 v146, v145
	v_sub_f32_e32 v136, v145, v137
	v_add_f32_e32 v137, v138, v139
	v_sub_f32_e32 v131, v131, v136
	v_mul_f32_e32 v148, v137, v146
	v_sub_f32_e32 v136, v137, v138
	v_mul_f32_e32 v138, v145, v148
	v_fma_f32 v140, v148, v145, -v138
	v_fmac_f32_e32 v140, v148, v131
	v_sub_f32_e32 v147, v139, v136
	v_add_f32_e32 v136, v138, v140
	v_sub_f32_e32 v139, v137, v136
	v_pk_add_f32 v[142:143], v[136:137], v[138:139] neg_lo:[0,1] neg_hi:[0,1]
	v_mov_b32_e32 v141, v136
	v_pk_add_f32 v[136:137], v[142:143], v[140:141] neg_lo:[0,1] neg_hi:[0,1]
	v_cmp_neq_f32_e32 vcc, s38, v133
	v_add_f32_e32 v137, v147, v137
	v_add_f32_e32 v136, v136, v137
	v_add_f32_e32 v137, v139, v136
	v_mul_f32_e32 v147, v146, v137
	v_mul_f32_e32 v138, v145, v147
	v_fma_f32 v140, v147, v145, -v138
	v_fmac_f32_e32 v140, v147, v131
	v_sub_f32_e32 v131, v139, v137
	v_add_f32_e32 v131, v136, v131
	v_add_f32_e32 v136, v138, v140
	v_sub_f32_e32 v139, v137, v136
	v_pk_add_f32 v[142:143], v[136:137], v[138:139] neg_lo:[0,1] neg_hi:[0,1]
	v_mov_b32_e32 v141, v136
	v_pk_add_f32 v[136:137], v[142:143], v[140:141] neg_lo:[0,1] neg_hi:[0,1]
	s_nop 0
	v_add_f32_e32 v131, v131, v137
	v_add_f32_e32 v131, v136, v131
	v_add_f32_e32 v137, v148, v147
	v_add_f32_e32 v131, v139, v131
	v_sub_f32_e32 v136, v137, v148
	v_mul_f32_e32 v131, v146, v131
	v_sub_f32_e32 v136, v147, v136
	v_add_f32_e32 v138, v136, v131
	v_add_f32_e32 v140, v137, v138
	v_cvt_f32_i32_e32 v136, v144
	v_mul_f32_e32 v141, v140, v140
	v_sub_f32_e32 v137, v140, v137
	v_fmamk_f32 v131, v141, 0x3e9b6dac, v181
	v_sub_f32_e32 v137, v138, v137
	v_fmaak_f32 v131, v141, v131, 0x3f2aaada
	v_ldexp_f32 v142, v137, 1
	v_mul_f32_e32 v137, v140, v141
	v_ldexp_f32 v139, v140, 1
	v_pk_mul_f32 v[140:141], v[136:137], v[130:131]
	s_nop 0
	v_fma_f32 v138, v136, s37, -v140
	v_fmac_f32_e32 v138, 0xb102e308, v136
	v_pk_add_f32 v[136:137], v[140:141], v[138:139]
	s_nop 0
	v_sub_f32_e32 v131, v137, v139
	v_sub_f32_e32 v131, v141, v131
	v_add_f32_e32 v143, v142, v131
	v_mov_b32_e32 v142, v140
	v_pk_add_f32 v[140:141], v[136:137], v[140:141] neg_lo:[0,1] neg_hi:[0,1]
	v_pk_add_f32 v[144:145], v[136:137], v[142:143]
	v_mov_b32_e32 v139, v136
	v_mov_b32_e32 v141, v145
	v_pk_add_f32 v[146:147], v[138:139], v[140:141] neg_lo:[0,1] neg_hi:[0,1]
	v_pk_add_f32 v[138:139], v[138:139], v[140:141]
	v_mov_b32_e32 v142, v143
	v_pk_add_f32 v[140:141], v[138:139], v[136:137] op_sel:[1,0] op_sel_hi:[0,1] neg_lo:[0,1] neg_hi:[0,1]
	v_pk_add_f32 v[148:149], v[144:145], v[140:141] op_sel_hi:[1,0] neg_lo:[0,1] neg_hi:[0,1]
	v_mov_b32_e32 v144, v145
	v_mov_b32_e32 v145, v139
	v_pk_mov_b32 v[140:141], v[136:137], v[140:141] op_sel:[1,0]
	v_mov_b32_e32 v143, v136
	v_pk_add_f32 v[140:141], v[144:145], v[140:141] neg_lo:[0,1] neg_hi:[0,1]
	v_mov_b32_e32 v148, v146
	v_pk_add_f32 v[136:137], v[142:143], v[140:141] neg_lo:[0,1] neg_hi:[0,1]
	v_mov_b32_e32 v147, v139
	v_pk_add_f32 v[140:141], v[148:149], v[136:137]
	s_nop 0
	v_pk_add_f32 v[142:143], v[140:141], v[140:141] op_sel:[0,1] op_sel_hi:[1,0]
	s_nop 0
	v_pk_add_f32 v[138:139], v[138:139], v[142:143] op_sel:[1,0] op_sel_hi:[0,1]
	v_mov_b32_e32 v141, v138
	v_pk_add_f32 v[144:145], v[140:141], v[146:147] neg_lo:[0,1] neg_hi:[0,1]
	v_mov_b32_e32 v137, v142
	v_sub_f32_e32 v131, v140, v144
	v_pk_add_f32 v[136:137], v[136:137], v[144:145] neg_lo:[0,1] neg_hi:[0,1]
	v_sub_f32_e32 v131, v146, v131
	v_add_f32_e32 v131, v136, v131
	v_add_f32_e32 v131, v131, v137
	v_add_f32_e32 v131, v138, v131
	v_cndmask_b32_e32 v131, v182, v131, vcc
	v_cmp_ngt_f32_e32 vcc, -1.0, v133
	s_nop 1
	v_cndmask_b32_e32 v131, v183, v131, vcc
	v_cmp_neq_f32_e32 vcc, -1.0, v133
	s_nop 1
	v_cndmask_b32_e32 v131, v184, v131, vcc
	v_cmp_lt_f32_e64 vcc, |v133|, s39
	s_nop 1
	v_cndmask_b32_e32 v138, v131, v133, vcc
; __device__ __forceinline__ float sigmoidf_(float x) { return __builtin_amdgcn_rcpf(1.f + __expf(-x)); }
; template <bool FINAL>
; __device__ __forceinline__ void lru_unit(const Args& a, unsigned char* lds_g, int b, int cidx, int blk, int tid, bf16x8_t (&wl)[2][2][4], int& wl_blk) {
;     ...
;             for (int r = 0; r < 4; ++r) { const float rr = sigmoidf_(acc[d][0][mt][r] + ba), ii = sigmoidf_(acc[d][1][mt][r] + bx);
;                 const float aa = __expf(-8.f * rr * sp); av[mt][r] = aa; bv[mt][r] = __builtin_amdgcn_sqrtf(fmaxf(1.f - aa * aa, 0.f)) * ii * zf[(16 * mt + 4 * fq + r) * 132 + chl]; }
.LBB0_305:
	s_or_b64 exec, exec, s[4:5]
	v_mul_f32_e32 v138, 0xc138aa3b, v138
	v_fma_f32 v124, v124, s92, v135
	v_exp_f32_e32 v124, v124
	v_fma_f32 v126, v126, s92, v135
	v_exp_f32_e32 v126, v126
	v_add_f32_e32 v124, 1.0, v124
	v_rcp_f32_e32 v124, v124
	v_fma_f32 v120, v120, s92, v134
	v_add_f32_e32 v126, 1.0, v126
	v_rcp_f32_e32 v126, v126
	v_mul_f32_e32 v124, v138, v124
	v_exp_f32_e32 v124, v124
	v_mul_f32_e32 v126, v138, v126
	v_exp_f32_e32 v120, v120
	v_fma_f32 v122, v122, s92, v134
	v_exp_f32_e32 v139, v126
	v_lshl_add_u32 v131, v132, 2, 0
	v_fma_f32 v132, -v124, v124, 1.0
	v_exp_f32_e32 v122, v122
	v_add_f32_e32 v120, 1.0, v120
	v_max_f32_e32 v132, 0, v132
	v_rcp_f32_e32 v120, v120
	v_sqrt_f32_e32 v132, v132
	v_fma_f32 v125, v125, s92, v135
	v_fma_f32 v126, -v139, v139, 1.0
	v_fma_f32 v127, v127, s92, v135
	v_exp_f32_e32 v125, v125
	v_add_f32_e32 v122, 1.0, v122
	v_max_f32_e32 v126, 0, v126
	v_rcp_f32_e32 v122, v122
	v_sqrt_f32_e32 v126, v126
	v_exp_f32_e32 v127, v127
	v_mul_f32_e32 v132, v120, v132
	v_mad_u32_u24 v120, v190, s40, v131
	v_fma_f32 v121, v121, s92, v134
	ds_read_b32 v120, v120
	v_add_f32_e32 v125, 1.0, v125
	v_exp_f32_e32 v137, v121
	v_lshlrev_b32_e32 v136, 2, v190
	v_rcp_f32_e32 v133, v125
	v_mul_f32_e32 v122, v122, v126
	v_add_f32_e32 v126, 1.0, v127
	v_or_b32_e32 v121, 1, v136
	v_rcp_f32_e32 v126, v126
	v_fma_f32 v116, v116, s92, v135
	v_mad_u32_u24 v140, v121, s33, v131
	ds_read_b32 v125, v140 offset:1056
	s_waitcnt lgkmcnt(1)
	v_mul_f32_e32 v131, v120, v132
	v_add_f32_e32 v132, 1.0, v137
	v_fma_f32 v123, v123, s92, v134
	v_exp_f32_e32 v116, v116
	v_rcp_f32_e32 v141, v132
	v_mul_f32_e32 v132, v138, v133
	v_exp_f32_e32 v127, v123
	v_mul_f32_e32 v123, v138, v126
	v_fma_f32 v118, v118, s92, v135
	v_exp_f32_e32 v137, v132
	v_add_f32_e32 v116, 1.0, v116
	v_fma_f32 v117, v117, s92, v135
	v_exp_f32_e32 v123, v123
	v_rcp_f32_e32 v116, v116
	v_exp_f32_e32 v118, v118
	v_exp_f32_e32 v117, v117
	v_fma_f32 v132, -v137, v137, 1.0
	v_max_f32_e32 v132, 0, v132
	v_add_f32_e32 v126, 1.0, v127
	v_fma_f32 v127, -v123, v123, 1.0
	v_mul_f32_e32 v116, v138, v116
	v_add_f32_e32 v118, 1.0, v118
	v_sqrt_f32_e32 v142, v132
	ds_read2_b32 v[132:133], v140 offset1:132
	v_max_f32_e32 v127, 0, v127
	v_add_f32_e32 v117, 1.0, v117
	v_rcp_f32_e32 v118, v118
	v_rcp_f32_e32 v126, v126
	v_sqrt_f32_e32 v127, v127
	v_fma_f32 v112, v112, s92, v134
	v_rcp_f32_e32 v117, v117
	v_exp_f32_e32 v194, v116
	v_exp_f32_e32 v112, v112
	v_fma_f32 v113, v113, s92, v134
	v_mul_f32_e32 v118, v138, v118
	s_waitcnt lgkmcnt(0)
	v_mul_f32_e32 v163, v133, v122
	v_mul_f32_e32 v122, v126, v127
	v_exp_f32_e32 v126, v113
	v_mul_f32_e32 v113, v138, v117
	v_fma_f32 v116, -v194, v194, 1.0
	v_add_f32_e32 v112, 1.0, v112
	v_max_f32_e32 v116, 0, v116
	v_exp_f32_e32 v197, v118
	v_fma_f32 v118, v119, s92, v135
	v_fma_f32 v108, v108, s92, v135
	v_rcp_f32_e32 v112, v112
	v_sqrt_f32_e32 v116, v116
	v_exp_f32_e32 v117, v113
	v_exp_f32_e32 v118, v118
	v_exp_f32_e32 v108, v108
	v_mul_f32_e32 v116, v112, v116
	v_add_u32_e32 v112, 0x1e00, v140
	v_fma_f32 v127, -v117, v117, 1.0
	ds_read2_b32 v[112:113], v112 offset0:60 offset1:192
	v_add_f32_e32 v126, 1.0, v126
	v_max_f32_e32 v127, 0, v127
	v_add_f32_e32 v118, 1.0, v118
	v_add_f32_e32 v108, 1.0, v108
	v_rcp_f32_e32 v126, v126
	v_sqrt_f32_e32 v127, v127
	v_fma_f32 v114, v114, s92, v134
	v_rcp_f32_e32 v118, v118
	v_rcp_f32_e32 v108, v108
	v_exp_f32_e32 v114, v114
	v_fma_f32 v115, v115, s92, v134
	s_waitcnt lgkmcnt(0)
	v_mul_f32_e32 v196, v112, v116
	v_mul_f32_e32 v116, v126, v127
	v_exp_f32_e32 v119, v115
	v_mul_f32_e32 v115, v138, v118
	v_mul_f32_e32 v108, v138, v108
	v_mul_f32_e32 v198, v113, v116
	v_fma_f32 v116, -v197, v197, 1.0
	v_add_f32_e32 v114, 1.0, v114
	v_max_f32_e32 v116, 0, v116
	v_rcp_f32_e32 v114, v114
	v_sqrt_f32_e32 v116, v116
	v_exp_f32_e32 v199, v115
	v_exp_f32_e32 v150, v108
	v_fma_f32 v108, v109, s92, v135
	v_exp_f32_e32 v108, v108
	v_mul_f32_e32 v116, v114, v116
	v_add_u32_e32 v114, 0x2200, v140
	v_add_f32_e32 v118, 1.0, v119
	v_fma_f32 v119, -v199, v199, 1.0
	v_fma_f32 v104, v104, s92, v134
	ds_read2_b32 v[114:115], v114 offset0:68 offset1:200
	v_max_f32_e32 v119, 0, v119
	v_rcp_f32_e32 v118, v118
	v_sqrt_f32_e32 v126, v119
	v_exp_f32_e32 v104, v104
	v_add_f32_e32 v108, 1.0, v108
	v_rcp_f32_e32 v108, v108
	v_fma_f32 v109, -v150, v150, 1.0
	v_fma_f32 v105, v105, s92, v134
	v_fma_f32 v100, v100, s92, v135
	s_waitcnt lgkmcnt(0)
; __device__ __forceinline__ float sigmoidf_(float x) { return __builtin_amdgcn_rcpf(1.f + __expf(-x)); }
; template <bool FINAL>
; __device__ __forceinline__ void lru_unit(const Args& a, unsigned char* lds_g, int b, int cidx, int blk, int tid, bf16x8_t (&wl)[2][2][4], int& wl_blk) {
;     ...
;             for (int r = 0; r < 4; ++r) { const float rr = sigmoidf_(acc[d][0][mt][r] + ba), ii = sigmoidf_(acc[d][1][mt][r] + bx);
;                 const float aa = __expf(-8.f * rr * sp); av[mt][r] = aa; bv[mt][r] = __builtin_amdgcn_sqrtf(fmaxf(1.f - aa * aa, 0.f)) * ii * zf[(16 * mt + 4 * fq + r) * 132 + chl]; }
;         float Pe[4], Se[4], Pt[4], St[4];
; #pragma unroll
;         for (int mt = 0; mt < 4; ++mt) {
;             float P = 1.f, S = 0.f;
; #pragma unroll
;             for (int rr = 0; rr < 4; ++rr) { const int r = d ? 3 - rr : rr; S = av[mt][r] * S + bv[mt][r]; P = av[mt][r] * P; }
;             if (d == 0) {
;                 float p1 = __shfl_up(P, 16), s1 = __shfl_up(S, 16); if (fq >= 1) { S = P * s1 + S; P = P * p1; }
;                 p1 = __shfl_up(P, 32); s1 = __shfl_up(S, 32); if (fq >= 2) { S = P * s1 + S; P = P * p1; }
;                 Pe[mt] = __shfl_up(P, 16); Se[mt] = __shfl_up(S, 16); if (fq == 0) { Pe[mt] = 1.f; Se[mt] = 0.f; }
;                 Pt[mt] = __shfl(P, fr + 48); St[mt] = __shfl(S, fr + 48);
	v_mul_f32_e32 v119, v114, v116
	v_mul_f32_e32 v116, v118, v126
	v_add_f32_e32 v104, 1.0, v104
	v_max_f32_e32 v109, 0, v109
	v_mul_f32_e32 v200, v115, v116
	v_rcp_f32_e32 v104, v104
	v_exp_f32_e32 v116, v105
	v_mul_f32_e32 v105, v138, v108
	v_sqrt_f32_e32 v108, v109
	v_exp_f32_e32 v100, v100
	v_fma_f32 v96, v96, s92, v134
	v_mul_f32_e32 v151, v104, v108
	v_add_u32_e32 v104, 0x3f00, v140
	v_add_f32_e32 v100, 1.0, v100
	ds_read2_b32 v[126:127], v104 offset0:60 offset1:192
	v_fma_f32 v104, v110, s92, v135
	v_rcp_f32_e32 v100, v100
	v_exp_f32_e32 v104, v104
	v_exp_f32_e32 v96, v96
	v_mul_f32_e32 v100, v138, v100
	v_add_f32_e32 v104, 1.0, v104
	v_rcp_f32_e32 v104, v104
	v_exp_f32_e32 v156, v100
	v_fma_f32 v100, v101, s92, v135
	v_exp_f32_e32 v100, v100
	v_mul_f32_e32 v104, v138, v104
	v_fma_f32 v101, -v156, v156, 1.0
	v_fma_f32 v97, v97, s92, v134
	v_add_f32_e32 v96, 1.0, v96
	v_max_f32_e32 v101, 0, v101
	v_add_f32_e32 v100, 1.0, v100
	v_exp_f32_e32 v153, v104
	v_fma_f32 v104, v111, s92, v135
	v_rcp_f32_e32 v96, v96
	v_sqrt_f32_e32 v101, v101
	v_exp_f32_e32 v97, v97
	v_rcp_f32_e32 v100, v100
	v_exp_f32_e32 v104, v104
	v_mul_f32_e32 v157, v96, v101
	v_add_f32_e32 v101, 1.0, v97
	v_mul_f32_e32 v97, v138, v100
	v_fma_f32 v100, v102, s92, v135
	v_add_f32_e32 v104, 1.0, v104
	v_exp_f32_e32 v100, v100
	v_rcp_f32_e32 v104, v104
	v_fma_f32 v107, v107, s92, v134
	v_add_f32_e32 v100, 1.0, v100
	v_mul_f32_e32 v104, v138, v104
	v_rcp_f32_e32 v100, v100
	v_add_u32_e32 v96, 0x6000, v140
	v_exp_f32_e32 v107, v107
	v_exp_f32_e32 v155, v104
	v_exp_f32_e32 v97, v97
	ds_read2_b32 v[148:149], v96 offset0:60 offset1:192
	v_fma_f32 v96, v103, s92, v135
	v_mul_f32_e32 v100, v138, v100
	v_exp_f32_e32 v96, v96
	v_exp_f32_e32 v105, v105
	v_add_f32_e32 v104, 1.0, v107
	v_fma_f32 v107, -v155, v155, 1.0
	v_fma_f32 v102, -v97, v97, 1.0
	v_exp_f32_e32 v159, v100
	v_max_f32_e32 v107, 0, v107
	v_max_f32_e32 v102, 0, v102
	v_rcp_f32_e32 v104, v104
	v_sqrt_f32_e32 v107, v107
	v_rcp_f32_e32 v101, v101
	v_fma_f32 v98, v98, s92, v134
	v_sqrt_f32_e32 v100, v102
	v_add_f32_e32 v96, 1.0, v96
	v_add_f32_e32 v109, 1.0, v116
	v_fma_f32 v116, -v105, v105, 1.0
	v_rcp_f32_e32 v96, v96
	v_max_f32_e32 v116, 0, v116
	v_exp_f32_e32 v98, v98
	v_fma_f32 v102, -v159, v159, 1.0
	v_mul_f32_e32 v141, v141, v142
	v_rcp_f32_e32 v109, v109
	v_sqrt_f32_e32 v116, v116
	v_max_f32_e32 v102, 0, v102
	v_mul_f32_e32 v141, v132, v141
	v_mul_f32_e32 v110, v104, v107
	v_sqrt_f32_e32 v104, v102
	v_mul_f32_e32 v102, v101, v100
	v_fma_f32 v100, 0, v124, v131
	v_add_u32_e32 v101, -16, v185
	v_and_b32_e32 v103, 64, v185
	v_mul_f32_e32 v96, v138, v96
	v_fma_f32 v100, v137, v100, v141
	v_cmp_lt_i32_e32 vcc, v101, v103
	v_mul_f32_e32 v195, v125, v122
	v_add_f32_e32 v98, 1.0, v98
	v_fma_f32 v100, v139, v100, v163
	v_cndmask_b32_e32 v101, v101, v185, vcc
	v_mul_f32_e32 v108, v109, v116
	v_rcp_f32_e32 v98, v98
	v_fma_f32 v100, v123, v100, v195
	v_lshlrev_b32_e32 v116, 2, v101
	v_exp_f32_e32 v161, v96
	v_mul_f32_e32 v96, v124, v137
	ds_bpermute_b32 v101, v116, v100
	v_mul_f32_e32 v96, v139, v96
	v_mul_f32_e32 v96, v123, v96
	v_mul_f32_e32 v144, v98, v104
	ds_bpermute_b32 v104, v116, v96
	v_fma_f32 v98, v99, s92, v134
	s_waitcnt lgkmcnt(1)
	v_fma_f32 v101, v96, v101, v100
	v_cmp_gt_u32_e64 s[4:5], 16, v189
	v_exp_f32_e32 v98, v98
	v_fma_f32 v106, v106, s92, v134
	v_cndmask_b32_e64 v100, v101, v100, s[4:5]
	v_subrev_u32_e32 v101, 32, v185
	v_cmp_lt_i32_e32 vcc, v101, v103
	s_waitcnt lgkmcnt(0)
	v_mul_f32_e32 v104, v96, v104
	v_cndmask_b32_e32 v101, v101, v185, vcc
	v_exp_f32_e32 v106, v106
	v_fma_f32 v107, -v161, v161, 1.0
	v_cndmask_b32_e64 v96, v104, v96, s[4:5]
	v_lshlrev_b32_e32 v118, 2, v101
	v_add_f32_e32 v98, 1.0, v98
	v_max_f32_e32 v107, 0, v107
	ds_bpermute_b32 v101, v118, v100
	ds_bpermute_b32 v104, v118, v96
	v_rcp_f32_e32 v98, v98
	v_sqrt_f32_e32 v107, v107
	v_fma_f32 v109, -v153, v153, 1.0
	v_add_f32_e32 v106, 1.0, v106
	v_max_f32_e32 v109, 0, v109
	v_rcp_f32_e32 v106, v106
	v_sqrt_f32_e32 v109, v109
	v_add_u32_e32 v99, 0x6400, v140
	ds_read2_b32 v[146:147], v99 offset0:68 offset1:200
	v_mul_f32_e32 v134, v98, v107
	s_waitcnt lgkmcnt(2)
	v_fma_f32 v98, v96, v101, v100
	s_waitcnt lgkmcnt(1)
	v_mul_f32_e32 v99, v96, v104
	v_mul_f32_e32 v101, v194, v117
	v_fma_f32 v104, 0, v194, v196
	v_mul_f32_e32 v101, v197, v101
	v_fma_f32 v104, v117, v104, v198
	v_mul_f32_e32 v101, v199, v101
	v_fma_f32 v104, v197, v104, v119
	v_mul_f32_e32 v106, v106, v109
	v_add_u32_e32 v109, 0x4400, v140
	v_fma_f32 v104, v199, v104, v200
	ds_bpermute_b32 v107, v116, v101
	ds_read2_b32 v[142:143], v109 offset0:4 offset1:136
	ds_bpermute_b32 v109, v116, v104
	v_cmp_lt_u32_e32 vcc, 31, v189
	v_or_b32_e32 v202, 2, v136
	v_or_b32_e32 v203, 3, v136
	v_cndmask_b32_e32 v96, v96, v99, vcc
	v_or_b32_e32 v99, v103, v189
	s_waitcnt lgkmcnt(2)
	v_mul_f32_e32 v103, v101, v107
	v_cndmask_b32_e32 v98, v100, v98, vcc
	s_waitcnt lgkmcnt(0)
	v_fma_f32 v100, v101, v109, v104
	v_cndmask_b32_e64 v101, v103, v101, s[4:5]
	v_cndmask_b32_e64 v103, v100, v104, s[4:5]
	ds_bpermute_b32 v104, v118, v101
	ds_bpermute_b32 v100, v118, v103
	v_or_b32_e32 v122, 16, v136
	v_or_b32_e32 v204, 17, v136
	v_or_b32_e32 v205, 18, v136
	v_or_b32_e32 v206, 19, v136
	v_or_b32_e32 v207, 32, v136
	v_or_b32_e32 v208, 33, v136
	v_or_b32_e32 v209, 34, v136
	v_or_b32_e32 v210, 35, v136
	v_or_b32_e32 v211, 48, v136
	v_or_b32_e32 v212, 49, v136
	v_or_b32_e32 v213, 50, v136
	v_or_b32_e32 v214, 51, v136
	v_lshl_or_b32 v136, v99, 2, v186
	ds_bpermute_b32 v201, v136, v98
	s_waitcnt lgkmcnt(2)
	v_mul_f32_e32 v98, v101, v104
	v_cndmask_b32_e32 v135, v101, v98, vcc
	v_mul_f32_e32 v98, v150, v105
	ds_bpermute_b32 v162, v136, v96
	s_waitcnt lgkmcnt(2)
; __device__ __forceinline__ unsigned pk2(float lo, float hi) { return pg8::cvt_pk_bf16(lo, hi); }
; template <bool FINAL>
; __device__ __forceinline__ void lru_unit(const Args& a, unsigned char* lds_g, int b, int cidx, int blk, int tid, bf16x8_t (&wl)[2][2][4], int& wl_blk) {
;     ...
;         float Pe[4], Se[4], Pt[4], St[4];
; #pragma unroll
;         for (int mt = 0; mt < 4; ++mt) {
;             float P = 1.f, S = 0.f;
; #pragma unroll
;             for (int rr = 0; rr < 4; ++rr) { const int r = d ? 3 - rr : rr; S = av[mt][r] * S + bv[mt][r]; P = av[mt][r] * P; }
;             if (d == 0) {
;                 float p1 = __shfl_up(P, 16), s1 = __shfl_up(S, 16); if (fq >= 1) { S = P * s1 + S; P = P * p1; }
;                 p1 = __shfl_up(P, 32); s1 = __shfl_up(S, 32); if (fq >= 2) { S = P * s1 + S; P = P * p1; }
;                 Pe[mt] = __shfl_up(P, 16); Se[mt] = __shfl_up(S, 16); if (fq == 0) { Pe[mt] = 1.f; Se[mt] = 0.f; }
;                 Pt[mt] = __shfl(P, fr + 48); St[mt] = __shfl(S, fr + 48);
;             } else {
;                 float p1 = __shfl_down(P, 16), s1 = __shfl_down(S, 16); if (fq <= 2) { S = P * s1 + S; P = P * p1; }
;                 p1 = __shfl_down(P, 32); s1 = __shfl_down(S, 32); if (fq <= 1) { S = P * s1 + S; P = P * p1; }
;                 Pe[mt] = __shfl_down(P, 16); Se[mt] = __shfl_down(S, 16); if (fq == 3) { Pe[mt] = 1.f; Se[mt] = 0.f; }
;                 Pt[mt] = __shfl(P, fr); St[mt] = __shfl(S, fr);
;             }
;         }
;         float2* AGG = (float2*)(a.ws + WS_AGG) + ((size_t)(b * 2 + d) * 36) * 1024 + ch;
;         if (!FINAL) {
;             if (cidx >= 4) {
;                 unsigned* PS = (unsigned*)(a.ws + WS_PS) + ((size_t)(b * 2 + d) * NSTEP + 64 * cidx) * 1024 + ch;
; #pragma unroll
;                 for (int mt = 0; mt < 4; ++mt)
; #pragma unroll
;                     for (int r = 0; r < 4; ++r) PS[(size_t)(16 * mt + 4 * fq + r) * 1024] = pk2(1.f - av[mt][r], bv[mt][r]);
;             }
	v_fma_f32 v96, v101, v100, v103
	v_mul_f32_e32 v98, v153, v98
	v_mov_b32_e32 v100, v129
	v_mov_b32_e32 v101, v126
	v_mul_f32_e32 v138, v155, v98
	v_pk_mul_f32 v[98:99], v[150:151], v[100:101]
	v_mov_b32_e32 v104, v127
	v_pk_fma_f32 v[100:101], v[150:151], v[100:101], v[98:99] op_sel_hi:[1,1,0]
	v_mov_b32_e32 v152, v142
	v_mov_b32_e32 v109, v101
	v_pk_mul_f32 v[168:169], v[108:109], v[104:105]
	v_mov_b32_e32 v154, v143
	v_pk_fma_f32 v[100:101], v[108:109], v[104:105], v[168:169] op_sel_hi:[1,1,0]
	v_cndmask_b32_e32 v96, v103, v96, vcc
	v_mov_b32_e32 v107, v101
	v_pk_mul_f32 v[170:171], v[106:107], v[152:153]
	v_mov_b32_e32 v158, v146
	v_pk_fma_f32 v[100:101], v[106:107], v[152:153], v[170:171] op_sel_hi:[1,1,0]
	ds_bpermute_b32 v152, v136, v96
	v_mov_b32_e32 v111, v101
	v_pk_mul_f32 v[172:173], v[110:111], v[154:155]
	ds_bpermute_b32 v101, v116, v138
	v_add_f32_e32 v98, v172, v173
	ds_bpermute_b32 v100, v116, v98
	v_mov_b32_e32 v106, v129
	v_mov_b32_e32 v107, v148
	ds_bpermute_b32 v164, v136, v135
	v_mov_b32_e32 v160, v147
	s_waitcnt lgkmcnt(1)
	v_fma_f32 v96, v138, v100, v98
	v_mul_f32_e32 v100, v138, v101
	v_cndmask_b32_e64 v104, v100, v138, s[4:5]
	v_cndmask_b32_e64 v98, v96, v98, s[4:5]
	v_mul_f32_e32 v96, v156, v97
	v_pk_mul_f32 v[100:101], v[156:157], v[106:107]
	v_mul_f32_e32 v96, v159, v96
	v_pk_fma_f32 v[106:107], v[156:157], v[106:107], v[100:101] op_sel_hi:[1,1,0]
	v_mul_f32_e32 v110, v161, v96
	v_mov_b32_e32 v103, v107
	v_mov_b32_e32 v96, v149
	v_pk_mul_f32 v[174:175], v[102:103], v[96:97]
	ds_bpermute_b32 v108, v118, v104
	v_pk_fma_f32 v[102:103], v[102:103], v[96:97], v[174:175] op_sel_hi:[1,1,0]
	ds_bpermute_b32 v109, v118, v98
	v_mov_b32_e32 v145, v103
	v_pk_mul_f32 v[176:177], v[144:145], v[158:159]
	s_waitcnt lgkmcnt(1)
	v_mul_f32_e32 v106, v104, v108
	v_pk_fma_f32 v[102:103], v[144:145], v[158:159], v[176:177] op_sel_hi:[1,1,0]
	ds_bpermute_b32 v102, v116, v110
	v_mov_b32_e32 v135, v103
	v_pk_mul_f32 v[178:179], v[134:135], v[160:161]
	s_waitcnt lgkmcnt(1)
	v_fma_f32 v103, v104, v109, v98
	v_add_f32_e32 v96, v178, v179
	ds_bpermute_b32 v100, v116, v96
	s_waitcnt lgkmcnt(1)
	v_mul_f32_e32 v102, v110, v102
	v_cndmask_b32_e64 v102, v102, v110, s[4:5]
	v_cndmask_b32_e32 v104, v104, v106, vcc
	ds_bpermute_b32 v106, v118, v102
	s_waitcnt lgkmcnt(1)
	v_fma_f32 v100, v110, v100, v96
	v_cndmask_b32_e64 v96, v100, v96, s[4:5]
	ds_bpermute_b32 v100, v118, v96
	v_cndmask_b32_e32 v98, v98, v103, vcc
	ds_bpermute_b32 v165, v136, v98
	ds_bpermute_b32 v166, v136, v104
	s_lshl_b32 s0, s25, 1
	s_waitcnt lgkmcnt(2)
	v_fma_f32 v98, v102, v100, v96
	v_mul_f32_e32 v100, v102, v106
	v_cndmask_b32_e32 v100, v102, v100, vcc
	v_cndmask_b32_e32 v96, v96, v98, vcc
	ds_bpermute_b32 v167, v136, v100
	ds_bpermute_b32 v151, v136, v96
	s_cmp_gt_i32 s24, 3
	s_cselect_b64 s[8:9], -1, 0
	s_cmp_lt_i32 s24, 4
	v_lshlrev_b32_e32 v144, 12, v190
	v_lshlrev_b32_e32 v140, 10, v121
	v_lshlrev_b32_e32 v138, 10, v202
	v_lshlrev_b32_e32 v136, 10, v203
	v_lshlrev_b32_e32 v134, 10, v122
	v_lshlrev_b32_e32 v122, 10, v204
	v_lshlrev_b32_e32 v118, 10, v205
	v_lshlrev_b32_e32 v116, 10, v206
	v_lshlrev_b32_e32 v110, 10, v207
	v_lshlrev_b32_e32 v108, 10, v208
	v_lshlrev_b32_e32 v106, 10, v209
	v_lshlrev_b32_e32 v104, 10, v210
	v_lshlrev_b32_e32 v102, 10, v211
	v_lshlrev_b32_e32 v100, 10, v212
	v_lshlrev_b32_e32 v98, 10, v213
	v_lshlrev_b32_e32 v96, 10, v214
	s_cbranch_scc1 .LBB0_307
	s_mul_i32 s6, s0, 0x900
	s_mul_hi_i32 s1, s0, 0x900
	s_add_u32 s6, s6, s43
	s_addc_u32 s7, s1, 0
	s_lshl_b64 s[6:7], s[6:7], 12
	s_add_u32 s6, s47, s6
	s_addc_u32 s7, s64, s7
	v_lshl_add_u64 v[202:203], v[128:129], 2, s[6:7]
	v_sub_f32_e32 v103, 1.0, v124
	v_mov_b32_e32 v145, v129
	v_cvt_pk_bf16_f32 v103, v103, v131
	v_lshl_add_u64 v[204:205], v[144:145], 2, v[202:203]
	global_store_dword v[204:205], v103, off
	v_sub_f32_e32 v103, 1.0, v137
	v_cvt_pk_bf16_f32 v103, v103, v141
	v_mov_b32_e32 v141, v129
	v_lshl_add_u64 v[204:205], v[140:141], 2, v[202:203]
	global_store_dword v[204:205], v103, off
	v_sub_f32_e32 v103, 1.0, v139
	v_mov_b32_e32 v139, v129
	v_cvt_pk_bf16_f32 v103, v103, v163
	v_lshl_add_u64 v[204:205], v[138:139], 2, v[202:203]
	global_store_dword v[204:205], v103, off
	v_sub_f32_e32 v103, 1.0, v123
	v_mov_b32_e32 v137, v129
	v_cvt_pk_bf16_f32 v103, v103, v195
	v_lshl_add_u64 v[204:205], v[136:137], 2, v[202:203]
	global_store_dword v[204:205], v103, off
	v_sub_f32_e32 v103, 1.0, v194
	v_mov_b32_e32 v135, v129
	v_cvt_pk_bf16_f32 v103, v103, v196
	v_lshl_add_u64 v[194:195], v[134:135], 2, v[202:203]
	global_store_dword v[194:195], v103, off
	v_sub_f32_e32 v103, 1.0, v117
	v_mov_b32_e32 v123, v129
	v_cvt_pk_bf16_f32 v103, v103, v198
	v_lshl_add_u64 v[194:195], v[122:123], 2, v[202:203]
	global_store_dword v[194:195], v103, off
	v_sub_f32_e32 v103, 1.0, v197
	v_cvt_pk_bf16_f32 v103, v103, v119
	v_mov_b32_e32 v119, v129
	v_lshl_add_u64 v[194:195], v[118:119], 2, v[202:203]
	global_store_dword v[194:195], v103, off
	v_sub_f32_e32 v103, 1.0, v199
	v_mov_b32_e32 v117, v129
	v_cvt_pk_bf16_f32 v103, v103, v200
	v_lshl_add_u64 v[194:195], v[116:117], 2, v[202:203]
	global_store_dword v[194:195], v103, off
	v_sub_f32_e32 v103, 1.0, v150
	v_mov_b32_e32 v111, v129
	v_cvt_pk_bf16_f32 v99, v103, v99
	v_lshl_add_u64 v[194:195], v[110:111], 2, v[202:203]
	global_store_dword v[194:195], v99, off
	v_sub_f32_e32 v99, 1.0, v105
	v_mov_b32_e32 v109, v129
	v_cvt_pk_bf16_f32 v99, v99, v168
	v_lshl_add_u64 v[168:169], v[108:109], 2, v[202:203]
	global_store_dword v[168:169], v99, off
	v_sub_f32_e32 v99, 1.0, v153
	v_mov_b32_e32 v107, v129
	v_cvt_pk_bf16_f32 v99, v99, v170
	v_lshl_add_u64 v[168:169], v[106:107], 2, v[202:203]
	global_store_dword v[168:169], v99, off
	v_sub_f32_e32 v99, 1.0, v155
	v_mov_b32_e32 v105, v129
	v_cvt_pk_bf16_f32 v99, v99, v172
	v_lshl_add_u64 v[154:155], v[104:105], 2, v[202:203]
	global_store_dword v[154:155], v99, off
	v_sub_f32_e32 v99, 1.0, v156
	v_mov_b32_e32 v103, v129
	v_cvt_pk_bf16_f32 v99, v99, v101
	v_lshl_add_u64 v[154:155], v[102:103], 2, v[202:203]
	v_sub_f32_e32 v97, 1.0, v97
	v_mov_b32_e32 v101, v129
	global_store_dword v[154:155], v99, off
	v_cvt_pk_bf16_f32 v97, v97, v174
	v_lshl_add_u64 v[154:155], v[100:101], 2, v[202:203]
	global_store_dword v[154:155], v97, off
	v_sub_f32_e32 v97, 1.0, v159
	v_mov_b32_e32 v99, v129
	v_cvt_pk_bf16_f32 v97, v97, v176
	v_lshl_add_u64 v[154:155], v[98:99], 2, v[202:203]
	global_store_dword v[154:155], v97, off
	v_sub_f32_e32 v97, 1.0, v161
	v_cvt_pk_bf16_f32 v99, v97, v178
	v_mov_b32_e32 v97, v129
	v_lshl_add_u64 v[154:155], v[96:97], 2, v[202:203]
	global_store_dword v[154:155], v99, off

; __device__ __forceinline__ float sigmoidf_(float x) { return __builtin_amdgcn_rcpf(1.f + __expf(-x)); }
; template <bool FINAL>
; __device__ __forceinline__ void lru_unit(const Args& a, unsigned char* lds_g, int b, int cidx, int blk, int tid, bf16x8_t (&wl)[2][2][4], int& wl_blk) {
;     ...
;         const float ba = gba[d], bx = gbx[d], lam = glam[d];
;         const float sp = (-lam > 20.f) ? -lam : log1pf(__expf(-lam));
;         float av[4][4], bv[4][4];
; #pragma unroll
;         for (int mt = 0; mt < 4; ++mt)
; #pragma unroll
;             for (int r = 0; r < 4; ++r) { const float rr = sigmoidf_(acc[d][0][mt][r] + ba), ii = sigmoidf_(acc[d][1][mt][r] + bx);
;                 const float aa = __expf(-8.f * rr * sp); av[mt][r] = aa; bv[mt][r] = __builtin_amdgcn_sqrtf(fmaxf(1.f - aa * aa, 0.f)) * ii * zf[(16 * mt + 4 * fq + r) * 132 + chl]; }
.LBB0_311:
	s_or_b64 exec, exec, s[6:7]
	v_mul_f32_e32 v105, 0xc138aa3b, v105
	v_fma_f32 v76, v76, s92, v191
	v_exp_f32_e32 v76, v76
	v_fma_f32 v72, v72, s92, v192
	v_exp_f32_e32 v72, v72
	v_add_f32_e32 v76, 1.0, v76
	v_rcp_f32_e32 v76, v76
	v_fma_f32 v73, v73, s92, v192
	v_add_f32_e32 v72, 1.0, v72
	v_rcp_f32_e32 v72, v72
	v_mul_f32_e32 v76, v105, v76
	v_exp_f32_e32 v103, v76
	v_fma_f32 v76, v77, s92, v191
	v_exp_f32_e32 v76, v76
	v_fma_f32 v77, -v103, v103, 1.0
	v_max_f32_e32 v77, 0, v77
	v_sqrt_f32_e32 v77, v77
	v_add_f32_e32 v76, 1.0, v76
	v_rcp_f32_e32 v76, v76
	v_exp_f32_e32 v73, v73
	v_mul_f32_e32 v72, v72, v77
	v_mul_f32_e32 v76, v105, v76
	v_exp_f32_e32 v107, v76
	v_fma_f32 v76, v78, s92, v191
	v_exp_f32_e32 v76, v76
	v_fma_f32 v77, -v107, v107, 1.0
	v_add_f32_e32 v73, 1.0, v73
	v_max_f32_e32 v77, 0, v77
	v_add_f32_e32 v76, 1.0, v76
	v_rcp_f32_e32 v76, v76
	v_rcp_f32_e32 v73, v73
	v_fma_f32 v92, v92, s92, v191
	v_mul_f32_e32 v76, v105, v76
	v_exp_f32_e32 v131, v76
	v_sqrt_f32_e32 v76, v77
	v_exp_f32_e32 v92, v92
	v_mul_f32_e32 v111, v126, v72
	v_fma_f32 v74, v74, s92, v192
	v_mul_f32_e32 v72, v73, v76
	v_fma_f32 v73, v79, s92, v191
	v_exp_f32_e32 v73, v73
	v_add_f32_e32 v92, 1.0, v92
	v_rcp_f32_e32 v92, v92
	v_exp_f32_e32 v74, v74
	v_add_f32_e32 v73, 1.0, v73
	v_fma_f32 v93, v93, s92, v191
	v_fma_f32 v77, -v131, v131, 1.0
	v_rcp_f32_e32 v73, v73
	v_mul_f32_e32 v92, v105, v92
	v_add_f32_e32 v74, 1.0, v74
	v_max_f32_e32 v77, 0, v77
	v_exp_f32_e32 v93, v93
	v_rcp_f32_e32 v74, v74
	v_sqrt_f32_e32 v77, v77
	v_fma_f32 v88, v88, s92, v192
	v_exp_f32_e32 v121, v92
	v_mul_f32_e32 v73, v105, v73
	v_fma_f32 v68, v68, s92, v191
	v_exp_f32_e32 v88, v88
	v_add_f32_e32 v92, 1.0, v93
	v_mul_f32_e32 v109, v127, v72
	v_mul_f32_e32 v72, v74, v77
	v_fma_f32 v74, v75, s92, v192
	v_exp_f32_e32 v68, v68
	v_rcp_f32_e32 v92, v92
	v_exp_f32_e32 v127, v73
	v_fma_f32 v93, -v121, v121, 1.0
	v_exp_f32_e32 v74, v74
	v_add_f32_e32 v88, 1.0, v88
	v_max_f32_e32 v93, 0, v93
	v_rcp_f32_e32 v88, v88
	v_sqrt_f32_e32 v93, v93
	v_add_f32_e32 v68, 1.0, v68
	v_mul_f32_e32 v92, v105, v92
	v_fma_f32 v73, -v127, v127, 1.0
	v_rcp_f32_e32 v68, v68
	v_mul_f32_e32 v126, v142, v72
	v_add_f32_e32 v72, 1.0, v74
	v_max_f32_e32 v73, 0, v73
	v_fma_f32 v89, v89, s92, v192
	v_rcp_f32_e32 v72, v72
	v_sqrt_f32_e32 v73, v73
	v_exp_f32_e32 v97, v92
	v_mul_f32_e32 v92, v88, v93
	v_fma_f32 v93, v94, s92, v191
	v_exp_f32_e32 v89, v89
	v_mul_f32_e32 v68, v105, v68
	v_exp_f32_e32 v93, v93
	v_mul_f32_e32 v72, v72, v73
	v_fma_f32 v90, v90, s92, v192
	v_mul_f32_e32 v142, v143, v72
	v_exp_f32_e32 v143, v68
	v_fma_f32 v68, v69, s92, v191
	v_add_f32_e32 v88, 1.0, v89
	v_fma_f32 v89, -v97, v97, 1.0
	v_max_f32_e32 v89, 0, v89
	v_exp_f32_e32 v94, v90
	v_add_f32_e32 v90, 1.0, v93
	v_exp_f32_e32 v68, v68
	v_rcp_f32_e32 v88, v88
	v_sqrt_f32_e32 v89, v89
	v_rcp_f32_e32 v93, v90
	v_fma_f32 v84, v84, s92, v191
	v_add_f32_e32 v68, 1.0, v68
	v_mul_f32_e32 v90, v88, v89
	v_mul_f32_e32 v89, v105, v93
	v_fma_f32 v93, v95, s92, v191
	v_rcp_f32_e32 v68, v68
	v_exp_f32_e32 v84, v84
	v_exp_f32_e32 v93, v93
	v_mul_f32_e32 v68, v105, v68
	v_fma_f32 v64, v64, s92, v192
	v_add_f32_e32 v84, 1.0, v84
	v_add_f32_e32 v93, 1.0, v93
	v_rcp_f32_e32 v84, v84
	v_fma_f32 v65, v65, s92, v192
	v_rcp_f32_e32 v93, v93
	v_exp_f32_e32 v64, v64
	v_exp_f32_e32 v154, v68
	v_exp_f32_e32 v89, v89
	v_exp_f32_e32 v65, v65
	v_fma_f32 v69, -v143, v143, 1.0
	v_mul_f32_e32 v84, v105, v84
	v_max_f32_e32 v69, 0, v69
	v_mul_f32_e32 v93, v105, v93
	v_add_f32_e32 v64, 1.0, v64
	v_sqrt_f32_e32 v68, v69
	v_fma_f32 v69, -v154, v154, 1.0
	v_fma_f32 v70, v70, s92, v191
	v_add_f32_e32 v88, 1.0, v94
	v_fma_f32 v94, -v89, v89, 1.0
	v_fma_f32 v91, v91, s92, v192
	v_rcp_f32_e32 v64, v64
	v_add_f32_e32 v65, 1.0, v65
	v_max_f32_e32 v69, 0, v69
	v_max_f32_e32 v94, 0, v94
	v_exp_f32_e32 v99, v84
	v_fma_f32 v84, v85, s92, v191
	v_rcp_f32_e32 v65, v65
	v_sqrt_f32_e32 v69, v69
	v_exp_f32_e32 v70, v70
	v_rcp_f32_e32 v88, v88
	v_sqrt_f32_e32 v94, v94
	v_exp_f32_e32 v91, v91
	v_exp_f32_e32 v124, v93
	v_exp_f32_e32 v84, v84
	v_mul_f32_e32 v64, v64, v68
	v_mul_f32_e32 v148, v148, v64
	v_mul_f32_e32 v64, v65, v69
	v_add_f32_e32 v65, 1.0, v70
	v_mul_f32_e32 v94, v88, v94
	v_add_f32_e32 v88, 1.0, v91
	v_fma_f32 v91, -v124, v124, 1.0
	v_rcp_f32_e32 v65, v65
	v_max_f32_e32 v91, 0, v91
	v_add_f32_e32 v84, 1.0, v84
	v_fma_f32 v66, v66, s92, v192
	v_rcp_f32_e32 v88, v88
	v_sqrt_f32_e32 v91, v91
	v_fma_f32 v80, v80, s92, v192
	v_rcp_f32_e32 v84, v84
	v_exp_f32_e32 v66, v66
	v_exp_f32_e32 v80, v80
	v_fma_f32 v81, v81, s92, v192
	v_mul_f32_e32 v65, v105, v65
	s_waitcnt lgkmcnt(0)
; __device__ __forceinline__ float sigmoidf_(float x) { return __builtin_amdgcn_rcpf(1.f + __expf(-x)); }
; template <bool FINAL>
; __device__ __forceinline__ void lru_unit(const Args& a, unsigned char* lds_g, int b, int cidx, int blk, int tid, bf16x8_t (&wl)[2][2][4], int& wl_blk) {
;     ...
;             for (int r = 0; r < 4; ++r) { const float rr = sigmoidf_(acc[d][0][mt][r] + ba), ii = sigmoidf_(acc[d][1][mt][r] + bx);
;                 const float aa = __expf(-8.f * rr * sp); av[mt][r] = aa; bv[mt][r] = __builtin_amdgcn_sqrtf(fmaxf(1.f - aa * aa, 0.f)) * ii * zf[(16 * mt + 4 * fq + r) * 132 + chl]; }
;         float Pe[4], Se[4], Pt[4], St[4];
; #pragma unroll
;         for (int mt = 0; mt < 4; ++mt) {
;             float P = 1.f, S = 0.f;
; #pragma unroll
;             for (int rr = 0; rr < 4; ++rr) { const int r = d ? 3 - rr : rr; S = av[mt][r] * S + bv[mt][r]; P = av[mt][r] * P; }
;             if (d == 0) {
;                 float p1 = __shfl_up(P, 16), s1 = __shfl_up(S, 16); if (fq >= 1) { S = P * s1 + S; P = P * p1; }
;                 p1 = __shfl_up(P, 32); s1 = __shfl_up(S, 32); if (fq >= 2) { S = P * s1 + S; P = P * p1; }
;                 Pe[mt] = __shfl_up(P, 16); Se[mt] = __shfl_up(S, 16); if (fq == 0) { Pe[mt] = 1.f; Se[mt] = 0.f; }
;                 Pt[mt] = __shfl(P, fr + 48); St[mt] = __shfl(S, fr + 48);
;             } else {
;                 float p1 = __shfl_down(P, 16), s1 = __shfl_down(S, 16); if (fq <= 2) { S = P * s1 + S; P = P * p1; }
;                 p1 = __shfl_down(P, 32); s1 = __shfl_down(S, 32); if (fq <= 1) { S = P * s1 + S; P = P * p1; }
;                 Pe[mt] = __shfl_down(P, 16); Se[mt] = __shfl_down(S, 16); if (fq == 3) { Pe[mt] = 1.f; Se[mt] = 0.f; }
;                 Pt[mt] = __shfl(P, fr); St[mt] = __shfl(S, fr);
;             }
;         }
	v_mul_f32_e32 v151, v88, v91
	v_exp_f32_e32 v88, v81
	v_mul_f32_e32 v81, v105, v84
	v_fma_f32 v85, -v99, v99, 1.0
	v_exp_f32_e32 v155, v65
	v_mul_f32_e32 v149, v149, v64
	v_add_f32_e32 v64, 1.0, v66
	v_fma_f32 v66, v71, s92, v191
	v_add_f32_e32 v80, 1.0, v80
	v_max_f32_e32 v85, 0, v85
	v_fma_f32 v86, v86, s92, v191
	v_rcp_f32_e32 v80, v80
	v_sqrt_f32_e32 v85, v85
	v_exp_f32_e32 v81, v81
	v_exp_f32_e32 v66, v66
	v_exp_f32_e32 v86, v86
	v_fma_f32 v65, -v155, v155, 1.0
	v_fma_f32 v67, v67, s92, v192
	v_max_f32_e32 v65, 0, v65
	v_mul_f32_e32 v84, v80, v85
	v_fma_f32 v85, -v81, v81, 1.0
	v_fma_f32 v82, v82, s92, v192
	v_rcp_f32_e32 v64, v64
	v_sqrt_f32_e32 v65, v65
	v_exp_f32_e32 v67, v67
	v_add_f32_e32 v66, 1.0, v66
	v_add_f32_e32 v80, 1.0, v88
	v_max_f32_e32 v85, 0, v85
	v_add_f32_e32 v86, 1.0, v86
	v_rcp_f32_e32 v66, v66
	v_rcp_f32_e32 v80, v80
	v_sqrt_f32_e32 v85, v85
	v_exp_f32_e32 v82, v82
	v_rcp_f32_e32 v88, v86
	v_mul_f32_e32 v68, v64, v65
	v_add_f32_e32 v64, 1.0, v67
	v_rcp_f32_e32 v69, v64
	v_mul_f32_e32 v64, v105, v66
	v_mul_f32_e32 v86, v80, v85
	v_add_f32_e32 v80, 1.0, v82
	v_mul_f32_e32 v82, v105, v88
	v_exp_f32_e32 v156, v64
	v_mul_f32_e32 v64, v124, v89
	v_mov_b32_e32 v150, v129
	v_exp_f32_e32 v101, v82
	v_fma_f32 v82, v87, s92, v191
	v_mul_f32_e32 v64, v97, v64
	v_pk_mul_f32 v[66:67], v[124:125], v[150:151]
	v_mul_f32_e32 v74, v121, v64
	v_pk_fma_f32 v[64:65], v[124:125], v[150:151], v[66:67] op_sel_hi:[1,1,0]
	v_exp_f32_e32 v82, v82
	v_mov_b32_e32 v88, v133
	v_mov_b32_e32 v95, v65
	v_pk_mul_f32 v[70:71], v[88:89], v[94:95]
	v_mov_b32_e32 v133, v97
	v_pk_fma_f32 v[64:65], v[88:89], v[94:95], v[70:71] op_sel_hi:[1,1,0]
	v_add_f32_e32 v82, 1.0, v82
	v_mov_b32_e32 v91, v65
	v_pk_mul_f32 v[72:73], v[132:133], v[90:91]
	v_rcp_f32_e32 v82, v82
	v_pk_fma_f32 v[64:65], v[132:133], v[90:91], v[72:73] op_sel_hi:[1,1,0]
	v_fma_f32 v85, -v101, v101, 1.0
	v_mov_b32_e32 v93, v65
	v_and_b32_e32 v65, 48, v185
	v_cmp_eq_u32_e32 vcc, 48, v65
	v_pk_mul_f32 v[76:77], v[120:121], v[92:93]
	v_mul_f32_e32 v82, v105, v82
	v_cndmask_b32_e64 v65, 16, 0, vcc
	v_add_f32_e32 v64, v76, v77
	v_add_lshl_u32 v77, v65, v185, 2
	v_fma_f32 v83, v83, s92, v192
	ds_bpermute_b32 v65, v77, v64
	v_max_f32_e32 v85, 0, v85
	v_rcp_f32_e32 v80, v80
	v_sqrt_f32_e32 v85, v85
	v_exp_f32_e32 v83, v83
	v_exp_f32_e32 v82, v82
	ds_bpermute_b32 v66, v77, v74
	v_fma_f32 v71, -v156, v156, 1.0
	s_waitcnt lgkmcnt(1)
	v_fma_f32 v65, v74, v65, v64
	v_cmp_eq_u32_e32 vcc, 3, v190
	v_mul_f32_e32 v152, v80, v85
	v_add_f32_e32 v80, 1.0, v83
	v_fma_f32 v83, -v82, v82, 1.0
	v_max_f32_e32 v71, 0, v71
	v_cndmask_b32_e32 v88, v65, v64, vcc
	v_max_f32_e32 v83, 0, v83
	v_sqrt_f32_e32 v71, v71
	s_waitcnt lgkmcnt(0)
	v_mul_f32_e32 v66, v74, v66
	ds_bpermute_b32 v64, v187, v88
	v_rcp_f32_e32 v80, v80
	v_sqrt_f32_e32 v83, v83
	v_cndmask_b32_e32 v66, v66, v74, vcc
	ds_bpermute_b32 v65, v187, v66
	v_mul_f32_e32 v73, v146, v68
	v_mul_f32_e32 v68, v69, v71
	v_mul_f32_e32 v159, v80, v83
	v_mul_f32_e32 v71, v147, v68
	s_waitcnt lgkmcnt(1)
	v_fma_f32 v68, v66, v64, v88
	v_mul_f32_e32 v64, v82, v101
	v_mov_b32_e32 v83, v115
	v_mov_b32_e32 v158, v129
	v_mul_f32_e32 v64, v81, v64
	v_pk_mul_f32 v[74:75], v[82:83], v[158:159]
	s_waitcnt lgkmcnt(0)
	v_mul_f32_e32 v69, v66, v65
	v_mul_f32_e32 v92, v99, v64
	v_pk_fma_f32 v[64:65], v[82:83], v[158:159], v[74:75] op_sel_hi:[1,1,0]
	v_mov_b32_e32 v115, v101
	v_mov_b32_e32 v153, v65
	v_pk_mul_f32 v[78:79], v[114:115], v[152:153]
	v_mov_b32_e32 v80, v113
	v_pk_fma_f32 v[64:65], v[114:115], v[152:153], v[78:79] op_sel_hi:[1,1,0]
	v_mov_b32_e32 v113, v99
	v_mov_b32_e32 v87, v65
	v_pk_mul_f32 v[90:91], v[80:81], v[86:87]
	v_cmp_gt_u32_e64 s[6:7], 32, v189
	v_pk_fma_f32 v[64:65], v[80:81], v[86:87], v[90:91] op_sel_hi:[1,1,0]
	s_or_b32 s0, s0, 1
	v_mov_b32_e32 v85, v65
	v_pk_mul_f32 v[84:85], v[112:113], v[84:85]
	ds_bpermute_b32 v65, v77, v92
	v_add_f32_e32 v64, v84, v85
	ds_bpermute_b32 v74, v77, v64
	v_cndmask_b32_e64 v66, v66, v69, s[6:7]
	v_and_or_b32 v69, v185, 64, v188
	s_waitcnt lgkmcnt(1)
	v_mul_f32_e32 v65, v92, v65
	v_cndmask_b32_e32 v79, v65, v92, vcc
	s_waitcnt lgkmcnt(0)
	v_fma_f32 v74, v92, v74, v64
	v_cndmask_b32_e32 v74, v74, v64, vcc
	ds_bpermute_b32 v83, v187, v79
	ds_bpermute_b32 v80, v187, v74
	v_cndmask_b32_e64 v68, v88, v68, s[6:7]
	v_lshlrev_b32_e32 v85, 2, v69
	v_mul_f32_e32 v69, v127, v131
	ds_bpermute_b32 v65, v85, v68
	s_waitcnt lgkmcnt(2)
	v_mul_f32_e32 v68, v79, v83
	v_mul_f32_e32 v69, v107, v69
	ds_bpermute_b32 v64, v85, v66
	s_waitcnt lgkmcnt(2)
	v_fma_f32 v66, v79, v80, v74
	v_cndmask_b32_e64 v68, v79, v68, s[6:7]
	v_mul_f32_e32 v79, v103, v69
	v_fma_f32 v69, 0, v127, v142
	v_fma_f32 v69, v131, v69, v126
	v_fma_f32 v69, v107, v69, v109
	v_fma_f32 v80, v103, v69, v111
	ds_bpermute_b32 v86, v77, v79
	ds_bpermute_b32 v83, v77, v80
	v_cndmask_b32_e64 v69, v74, v66, s[6:7]
	ds_bpermute_b32 v66, v85, v68
	ds_bpermute_b32 v69, v85, v69
	s_waitcnt lgkmcnt(3)
	v_mul_f32_e32 v74, v79, v86
	v_fma_f32 v86, 0, v156, v71
	s_waitcnt lgkmcnt(2)
	v_fma_f32 v68, v79, v83, v80
	v_mul_f32_e32 v83, v156, v155
	v_fma_f32 v86, v155, v86, v73
	v_cndmask_b32_e32 v74, v74, v79, vcc
	v_mul_f32_e32 v83, v154, v83
	v_fma_f32 v86, v154, v86, v149
	v_cndmask_b32_e32 v68, v68, v80, vcc
	ds_bpermute_b32 v79, v187, v74
	v_mul_f32_e32 v83, v143, v83
	v_fma_f32 v86, v143, v86, v148
	ds_bpermute_b32 v80, v187, v68
	ds_bpermute_b32 v87, v77, v86
	ds_bpermute_b32 v77, v77, v83
	s_waitcnt lgkmcnt(3)
	v_mul_f32_e32 v79, v74, v79
	s_waitcnt lgkmcnt(2)
	v_fma_f32 v80, v74, v80, v68
	v_cndmask_b32_e64 v74, v74, v79, s[6:7]
	s_waitcnt lgkmcnt(1)
	v_fma_f32 v79, v83, v87, v86
	s_waitcnt lgkmcnt(0)
	v_mul_f32_e32 v77, v83, v77
	v_cndmask_b32_e32 v83, v77, v83, vcc
	v_cndmask_b32_e32 v79, v79, v86, vcc
	ds_bpermute_b32 v86, v187, v79
	ds_bpermute_b32 v87, v187, v83
	v_cndmask_b32_e64 v68, v68, v80, s[6:7]
	ds_bpermute_b32 v77, v85, v68
	ds_bpermute_b32 v74, v85, v74
	s_waitcnt lgkmcnt(3)
	v_fma_f32 v68, v83, v86, v79
	s_waitcnt lgkmcnt(2)
	v_mul_f32_e32 v80, v83, v87
	v_cndmask_b32_e64 v80, v83, v80, s[6:7]
	v_cndmask_b32_e64 v79, v79, v68, s[6:7]
	ds_bpermute_b32 v68, v85, v80
	ds_bpermute_b32 v79, v85, v79
	s_andn2_b64 vcc, exec, s[8:9]
	s_cbranch_vccnz .LBB0_313
; __device__ __forceinline__ unsigned pk2(float lo, float hi) { return pg8::cvt_pk_bf16(lo, hi); }
; template <bool FINAL>
; __device__ __forceinline__ void lru_unit(const Args& a, unsigned char* lds_g, int b, int cidx, int blk, int tid, bf16x8_t (&wl)[2][2][4], int& wl_blk) {
;     ...
;         if (!FINAL) {
;             if (cidx >= 4) {
;                 unsigned* PS = (unsigned*)(a.ws + WS_PS) + ((size_t)(b * 2 + d) * NSTEP + 64 * cidx) * 1024 + ch;
; #pragma unroll
;                 for (int mt = 0; mt < 4; ++mt)
; #pragma unroll
;                     for (int r = 0; r < 4; ++r) PS[(size_t)(16 * mt + 4 * fq + r) * 1024] = pk2(1.f - av[mt][r], bv[mt][r]);
;             }
	s_mul_i32 s6, s0, 0x900
	s_mul_hi_i32 s1, s0, 0x900
	s_add_u32 s6, s6, s43
	s_addc_u32 s7, s1, 0
	s_lshl_b64 s[6:7], s[6:7], 12
	s_add_u32 s6, s47, s6
	s_addc_u32 s7, s64, s7
	v_lshl_add_u64 v[86:87], v[128:129], 2, s[6:7]
	v_sub_f32_e32 v80, 1.0, v121
	v_mov_b32_e32 v145, v129
	v_cvt_pk_bf16_f32 v76, v80, v76
	v_lshl_add_u64 v[92:93], v[144:145], 2, v[86:87]
	global_store_dword v[92:93], v76, off
	v_sub_f32_e32 v76, 1.0, v97
	v_mov_b32_e32 v141, v129
	v_cvt_pk_bf16_f32 v72, v76, v72
	v_lshl_add_u64 v[92:93], v[140:141], 2, v[86:87]
	global_store_dword v[92:93], v72, off
	v_sub_f32_e32 v72, 1.0, v89
	v_mov_b32_e32 v139, v129
	v_cvt_pk_bf16_f32 v70, v72, v70
	v_lshl_add_u64 v[88:89], v[138:139], 2, v[86:87]
	global_store_dword v[88:89], v70, off
	v_sub_f32_e32 v70, 1.0, v124
	v_mov_b32_e32 v137, v129
	v_cvt_pk_bf16_f32 v67, v70, v67
	v_lshl_add_u64 v[88:89], v[136:137], 2, v[86:87]
	global_store_dword v[88:89], v67, off
	v_sub_f32_e32 v67, 1.0, v99
	v_mov_b32_e32 v135, v129
	v_cvt_pk_bf16_f32 v67, v67, v84
	v_lshl_add_u64 v[84:85], v[134:135], 2, v[86:87]
	global_store_dword v[84:85], v67, off
	v_sub_f32_e32 v67, 1.0, v81
	v_mov_b32_e32 v123, v129
	v_cvt_pk_bf16_f32 v67, v67, v90
	v_lshl_add_u64 v[80:81], v[122:123], 2, v[86:87]
	global_store_dword v[80:81], v67, off
	v_sub_f32_e32 v67, 1.0, v101
	v_mov_b32_e32 v119, v129
	v_cvt_pk_bf16_f32 v67, v67, v78
	v_lshl_add_u64 v[80:81], v[118:119], 2, v[86:87]
	global_store_dword v[80:81], v67, off
	v_sub_f32_e32 v67, 1.0, v82
	v_mov_b32_e32 v117, v129
	v_cvt_pk_bf16_f32 v67, v67, v75
	v_lshl_add_u64 v[80:81], v[116:117], 2, v[86:87]
	global_store_dword v[80:81], v67, off
	v_sub_f32_e32 v67, 1.0, v103
	v_cvt_pk_bf16_f32 v67, v67, v111
	v_mov_b32_e32 v111, v129
	v_lshl_add_u64 v[80:81], v[110:111], 2, v[86:87]
	global_store_dword v[80:81], v67, off
	v_sub_f32_e32 v67, 1.0, v107
	v_cvt_pk_bf16_f32 v67, v67, v109
	v_mov_b32_e32 v109, v129
	v_lshl_add_u64 v[80:81], v[108:109], 2, v[86:87]
	global_store_dword v[80:81], v67, off
	v_sub_f32_e32 v67, 1.0, v131
	v_mov_b32_e32 v107, v129
	v_cvt_pk_bf16_f32 v67, v67, v126
	v_lshl_add_u64 v[80:81], v[106:107], 2, v[86:87]
	global_store_dword v[80:81], v67, off
	v_sub_f32_e32 v67, 1.0, v127
	v_mov_b32_e32 v105, v129
	v_cvt_pk_bf16_f32 v67, v67, v142
	v_lshl_add_u64 v[80:81], v[104:105], 2, v[86:87]
	global_store_dword v[80:81], v67, off
	v_sub_f32_e32 v67, 1.0, v143
	v_mov_b32_e32 v103, v129
	v_cvt_pk_bf16_f32 v67, v67, v148
	v_lshl_add_u64 v[80:81], v[102:103], 2, v[86:87]
	global_store_dword v[80:81], v67, off
	v_sub_f32_e32 v67, 1.0, v154
	v_mov_b32_e32 v101, v129
	v_cvt_pk_bf16_f32 v67, v67, v149
	v_lshl_add_u64 v[80:81], v[100:101], 2, v[86:87]
	global_store_dword v[80:81], v67, off
	v_sub_f32_e32 v67, 1.0, v155
	v_mov_b32_e32 v99, v129
	v_cvt_pk_bf16_f32 v67, v67, v73
	v_lshl_add_u64 v[72:73], v[98:99], 2, v[86:87]
	global_store_dword v[72:73], v67, off
	v_sub_f32_e32 v67, 1.0, v156
	v_mov_b32_e32 v97, v129
	v_cvt_pk_bf16_f32 v67, v67, v71
	v_lshl_add_u64 v[70:71], v[96:97], 2, v[86:87]
	global_store_dword v[70:71], v67, off
